# rwkv pass C finalize: the 64 serialized bf16 bonus/gate loads issued together up front, per-load waits dropped (on top of v20)
# speedup vs baseline: 1.1154x; 1.0030x over previous
.LBB0_1483:
	s_bfe_u32 s0, s7, 0x20006
	s_cmp_gt_i32 s13, 3
	s_cselect_b32 s1, 0x107, 3
	s_ashr_i32 s7, s7, 3
	s_sub_i32 s1, s1, s13
	s_andn2_b32 s7, s7, 31
	s_ashr_i32 s16, s13, 31
	s_mul_hi_i32 s15, s6, 0x104
	s_add_u32 s14, s5, s13
	v_and_b32_e32 v100, 15, v2
	s_addc_u32 s15, s15, s16
	v_bfe_u32 v4, v2, 4, 2
	v_lshlrev_b32_e32 v82, 7, v100
	s_lshl_b64 s[14:15], s[14:15], 2
	v_lshl_add_u64 v[2:3], s[2:3], 0, v[82:83]
	v_lshlrev_b32_e32 v82, 4, v4
	s_or_b32 s14, s14, s0
	v_lshl_add_u64 v[50:51], v[2:3], 0, v[82:83]
	s_lshl_b64 s[16:17], s[14:15], 14
	v_lshl_add_u64 v[2:3], v[50:51], 0, s[16:17]
	global_load_dwordx4 v[42:45], v[2:3], off
	global_load_dwordx4 v[46:49], v[2:3], off offset:64
	global_load_dwordx4 v[26:29], v[2:3], off offset:2048
	global_load_dwordx4 v[30:33], v[2:3], off offset:2112
	v_add_co_u32_e32 v2, vcc, s62, v2
	s_lshl_b64 s[14:15], s[14:15], 15
	s_nop 0
	v_addc_co_u32_e32 v3, vcc, 0, v3, vcc
	s_add_u32 s14, s9, s14
	global_load_dwordx4 v[34:37], v[2:3], off
	global_load_dwordx4 v[38:41], v[2:3], off offset:64
	global_load_dwordx4 v[18:21], v[2:3], off offset:2048
	global_load_dwordx4 v[22:25], v[2:3], off offset:2112
	v_or_b32_e32 v2, s7, v100
	s_addc_u32 s15, s10, s15
	v_lshlrev_b32_e32 v82, 5, v4
	v_lshlrev_b32_e32 v90, 6, v2
	v_lshl_add_u64 v[60:61], s[14:15], 0, v[82:83]
	v_ashrrev_i32_e32 v91, 31, v90
	v_lshl_add_u64 v[10:11], v[90:91], 2, v[60:61]
	v_lshlrev_b32_e32 v72, 2, v4
	global_load_dwordx4 v[2:5], v[10:11], off offset:16
	global_load_dwordx4 v[6:9], v[10:11], off
	v_lshlrev_b32_e32 v96, 8, v100
	v_mov_b32_e32 v97, v83
	v_or_b32_e32 v84, s7, v72
	v_lshl_add_u64 v[58:59], s[14:15], 0, v[96:97]
	v_ashrrev_i32_e32 v85, 31, v84
	v_lshl_add_u64 v[52:53], v[58:59], 0, s[18:19]
	v_lshlrev_b64 v[86:87], 2, v[84:85]
	s_mov_b64 s[16:17], 0x5000
	v_lshl_add_u64 v[54:55], v[58:59], 0, s[16:17]
	s_mov_b64 s[20:21], 0x6000
	v_lshl_add_u64 v[56:57], v[58:59], 0, s[20:21]
	s_mov_b64 s[22:23], 0x7000
	v_lshl_add_u64 v[58:59], v[58:59], 0, s[22:23]
	s_or_b32 s13, s7, 16
	s_ashr_i32 s7, s7, 31
	v_mov_b32_e32 v85, s7
	v_or_b32_e32 v92, s13, v72
	v_ashrrev_i32_e32 v93, 31, v92
	v_lshlrev_b64 v[94:95], 2, v[92:93]
	s_add_i32 s6, s6, 2
	s_addk_i32 s5, 0x208
	s_mul_hi_i32 s7, s6, 0x104
	s_add_u32 s6, s5, s1
	s_addc_u32 s7, s7, 0
	s_lshl_b64 s[6:7], s[6:7], 2
	s_or_b32 s6, s6, s0
	s_lshl_b64 s[14:15], s[6:7], 14
	s_lshl_b64 s[6:7], s[6:7], 15
	s_add_u32 s6, s9, s6
	s_addc_u32 s7, s10, s7
	v_lshl_add_u64 v[98:99], s[6:7], 0, v[82:83]
	s_lshl_b32 s1, s0, 6
	s_or_b32 s1, s1, s8
	v_or_b32_e32 v82, s1, v100
	s_lshl_b32 s50, s0, 7
	s_add_u32 s0, s11, s50
	s_addc_u32 s1, s12, 0
	s_movk_i32 s5, 0x7fff
	s_mov_b32 s80, 0x25bb0000
	s_waitcnt vmcnt(0)
	v_cvt_pk_bf16_f32 v62, v6, v7
	v_cvt_pk_bf16_f32 v63, v8, v9
	v_cvt_pk_bf16_f32 v64, v2, v3
	v_cvt_pk_bf16_f32 v65, v4, v5
	global_load_dwordx4 v[2:5], v[10:11], off offset:144
	global_load_dwordx4 v[6:9], v[10:11], off offset:128
	s_waitcnt vmcnt(0)
	v_cvt_pk_bf16_f32 v66, v6, v7
	v_cvt_pk_bf16_f32 v67, v8, v9
	v_cvt_pk_bf16_f32 v68, v2, v3
	v_lshl_add_u64 v[2:3], v[52:53], 0, v[86:87]
	v_cvt_pk_bf16_f32 v69, v4, v5
	global_load_dwordx4 v[2:5], v[2:3], off
	v_lshl_add_u64 v[52:53], v[84:85], 2, v[52:53]
	s_waitcnt vmcnt(0)
	v_mfma_f32_16x16x32_bf16 v[2:5], v[62:65], v[42:45], v[2:5]
	v_mfma_f32_16x16x32_bf16 v[14:17], v[66:69], v[46:49], v[2:5]
	s_nop 6
	v_lshl_add_u64 v[2:3], v[54:55], 0, v[86:87]
	global_load_dwordx4 v[2:5], v[2:3], off
	s_waitcnt vmcnt(0)
	v_mfma_f32_16x16x32_bf16 v[2:5], v[62:65], v[26:29], v[2:5]
	v_mfma_f32_16x16x32_bf16 v[10:13], v[66:69], v[30:33], v[2:5]
	s_nop 6
	v_lshl_add_u64 v[2:3], v[56:57], 0, v[86:87]
	global_load_dwordx4 v[2:5], v[2:3], off
	s_waitcnt vmcnt(0)
	v_mfma_f32_16x16x32_bf16 v[2:5], v[62:65], v[34:37], v[2:5]
	v_mfma_f32_16x16x32_bf16 v[6:9], v[66:69], v[38:41], v[2:5]
	s_nop 6
	v_lshl_add_u64 v[2:3], v[58:59], 0, v[86:87]
	global_load_dwordx4 v[2:5], v[2:3], off
	s_waitcnt vmcnt(0)
	v_mfma_f32_16x16x32_bf16 v[2:5], v[62:65], v[18:21], v[2:5]
	v_or_b32_e32 v62, s13, v100
	v_lshlrev_b32_e32 v88, 6, v62
	v_ashrrev_i32_e32 v89, 31, v88
	v_mfma_f32_16x16x32_bf16 v[2:5], v[66:69], v[22:25], v[2:5]
	v_lshl_add_u64 v[68:69], v[88:89], 2, v[60:61]
	global_load_dwordx4 v[60:63], v[68:69], off offset:16
	global_load_dwordx4 v[64:67], v[68:69], off
	s_waitcnt vmcnt(0)
	v_cvt_pk_bf16_f32 v64, v64, v65
	v_cvt_pk_bf16_f32 v65, v66, v67
	v_cvt_pk_bf16_f32 v66, v60, v61
	v_cvt_pk_bf16_f32 v67, v62, v63
	global_load_dwordx4 v[60:63], v[68:69], off offset:144
	s_nop 0
	global_load_dwordx4 v[68:71], v[68:69], off offset:128
	s_waitcnt vmcnt(0)
	v_cvt_pk_bf16_f32 v68, v68, v69
	v_cvt_pk_bf16_f32 v69, v70, v71
	v_cvt_pk_bf16_f32 v70, v60, v61
	v_cvt_pk_bf16_f32 v71, v62, v63
	global_load_dwordx4 v[60:63], v[52:53], off offset:64
	s_waitcnt vmcnt(0)
	v_mfma_f32_16x16x32_bf16 v[42:45], v[64:67], v[42:45], v[60:63]
	v_mfma_f32_16x16x32_bf16 v[46:49], v[68:71], v[46:49], v[42:45]
	s_nop 6
	v_lshl_add_u64 v[42:43], v[54:55], 0, v[94:95]
	global_load_dwordx4 v[42:45], v[42:43], off
	s_waitcnt vmcnt(0)
	v_mfma_f32_16x16x32_bf16 v[26:29], v[64:67], v[26:29], v[42:45]
	v_mfma_f32_16x16x32_bf16 v[42:45], v[68:71], v[30:33], v[26:29]
	v_lshl_add_u64 v[30:31], s[6:7], 0, v[96:97]
	v_lshl_add_u64 v[96:97], v[30:31], 0, s[18:19]
	v_lshl_add_u64 v[110:111], v[30:31], 0, s[20:21]
	s_nop 3
	v_lshl_add_u64 v[26:27], v[56:57], 0, v[94:95]
	global_load_dwordx4 v[26:29], v[26:27], off
	v_lshl_add_u64 v[112:113], v[30:31], 0, s[22:23]
	s_mov_b32 s6, 0x25bb0000
	s_waitcnt vmcnt(0)
	v_mfma_f32_16x16x32_bf16 v[26:29], v[64:67], v[34:37], v[26:29]
	v_mfma_f32_16x16x32_bf16 v[38:41], v[68:71], v[38:41], v[26:29]
	s_nop 6
	v_lshl_add_u64 v[26:27], v[58:59], 0, v[94:95]
	global_load_dwordx4 v[26:29], v[26:27], off
	s_waitcnt vmcnt(0)
	v_mfma_f32_16x16x32_bf16 v[18:21], v[64:67], v[18:21], v[26:29]
	v_mfma_f32_16x16x32_bf16 v[34:37], v[68:71], v[22:25], v[18:21]
	s_nop 6
	v_lshl_add_u64 v[18:19], v[50:51], 0, s[14:15]
	global_load_dwordx4 v[74:77], v[18:19], off
	global_load_dwordx4 v[78:81], v[18:19], off offset:64
	global_load_dwordx4 v[66:69], v[18:19], off offset:2048
	global_load_dwordx4 v[70:73], v[18:19], off offset:2112
	v_add_co_u32_e32 v18, vcc, s62, v18
	s_mov_b32 s14, 0x3c800000
	s_nop 0
	v_addc_co_u32_e32 v19, vcc, 0, v19, vcc
	global_load_dwordx4 v[58:61], v[18:19], off
	global_load_dwordx4 v[62:65], v[18:19], off offset:64
	global_load_dwordx4 v[50:53], v[18:19], off offset:2048
	global_load_dwordx4 v[54:57], v[18:19], off offset:2112
	v_sub_u32_e32 v18, 0xfc0, v90
	v_ashrrev_i32_e32 v19, 31, v18
	v_lshl_add_u64 v[26:27], v[18:19], 2, v[98:99]
	global_load_dwordx4 v[18:21], v[26:27], off offset:16
	global_load_dwordx4 v[22:25], v[26:27], off
	v_lshl_add_u64 v[90:91], v[30:31], 0, s[16:17]
	v_readlane_b32 s16, v253, 9
	v_readlane_b32 s17, v253, 10
	v_readlane_b32 s18, v253, 11
	v_readlane_b32 s19, v253, 12
	s_waitcnt vmcnt(0)
	v_cvt_pk_bf16_f32 v102, v22, v23
	v_cvt_pk_bf16_f32 v103, v24, v25
	v_cvt_pk_bf16_f32 v104, v18, v19
	v_cvt_pk_bf16_f32 v105, v20, v21
	global_load_dwordx4 v[18:21], v[26:27], off offset:144
	global_load_dwordx4 v[22:25], v[26:27], off offset:128
	s_waitcnt vmcnt(0)
	v_cvt_pk_bf16_f32 v106, v22, v23
	v_cvt_pk_bf16_f32 v107, v24, v25
	v_cvt_pk_bf16_f32 v108, v18, v19
	v_sub_co_u32_e32 v18, vcc, v96, v86
	v_cvt_pk_bf16_f32 v109, v20, v21
	v_sub_u32_e32 v22, 60, v84
	s_nop 0
	v_subb_co_u32_e32 v19, vcc, v97, v87, vcc
	global_load_dwordx4 v[18:21], v[18:19], off offset:240
	v_ashrrev_i32_e32 v23, 31, v22
	v_lshlrev_b64 v[32:33], 2, v[22:23]
	s_waitcnt vmcnt(0)
	v_pk_add_f32 v[14:15], v[14:15], v[20:21] op_sel:[0,1] op_sel_hi:[1,0]
	v_pk_add_f32 v[16:17], v[16:17], v[18:19] op_sel:[0,1] op_sel_hi:[1,0]
	s_nop 1
	v_mfma_f32_16x16x32_bf16 v[14:17], v[102:105], v[74:77], v[14:17]
	v_mfma_f32_16x16x32_bf16 v[18:21], v[106:109], v[78:81], v[14:17]
	s_nop 6
	v_lshl_add_u64 v[14:15], v[90:91], 0, v[32:33]
	global_load_dwordx4 v[14:17], v[14:15], off
	s_waitcnt vmcnt(0)
	v_pk_add_f32 v[10:11], v[10:11], v[16:17] op_sel:[0,1] op_sel_hi:[1,0]
	v_pk_add_f32 v[12:13], v[12:13], v[14:15] op_sel:[0,1] op_sel_hi:[1,0]
	s_nop 1
	v_mfma_f32_16x16x32_bf16 v[10:13], v[102:105], v[66:69], v[10:13]
	v_mfma_f32_16x16x32_bf16 v[22:25], v[106:109], v[70:73], v[10:13]
	s_nop 6
	v_lshl_add_u64 v[10:11], v[110:111], 0, v[32:33]
	global_load_dwordx4 v[10:13], v[10:11], off
	s_waitcnt vmcnt(0)
	v_pk_add_f32 v[6:7], v[6:7], v[12:13] op_sel:[0,1] op_sel_hi:[1,0]
	v_pk_add_f32 v[8:9], v[8:9], v[10:11] op_sel:[0,1] op_sel_hi:[1,0]
	s_nop 1
	v_mfma_f32_16x16x32_bf16 v[6:9], v[102:105], v[58:61], v[6:9]
	v_mfma_f32_16x16x32_bf16 v[26:29], v[106:109], v[62:65], v[6:9]
	s_nop 6
	v_lshl_add_u64 v[6:7], v[112:113], 0, v[32:33]
	global_load_dwordx4 v[6:9], v[6:7], off
	s_waitcnt vmcnt(0)
	v_pk_add_f32 v[2:3], v[2:3], v[8:9] op_sel:[0,1] op_sel_hi:[1,0]
	v_pk_add_f32 v[4:5], v[4:5], v[6:7] op_sel:[0,1] op_sel_hi:[1,0]
	s_nop 1
	v_mfma_f32_16x16x32_bf16 v[2:5], v[102:105], v[50:53], v[2:5]
	v_mfma_f32_16x16x32_bf16 v[30:33], v[106:109], v[54:57], v[2:5]
	s_nop 6
	v_sub_u32_e32 v2, 0xfc0, v88
	v_ashrrev_i32_e32 v3, 31, v2
	v_lshl_add_u64 v[10:11], v[2:3], 2, v[98:99]
	global_load_dwordx4 v[2:5], v[10:11], off offset:16
	global_load_dwordx4 v[6:9], v[10:11], off
	s_waitcnt vmcnt(0)
	v_cvt_pk_bf16_f32 v14, v6, v7
	v_cvt_pk_bf16_f32 v15, v8, v9
	v_cvt_pk_bf16_f32 v16, v2, v3
	v_cvt_pk_bf16_f32 v17, v4, v5
	global_load_dwordx4 v[2:5], v[10:11], off offset:144
	global_load_dwordx4 v[6:9], v[10:11], off offset:128
	s_waitcnt vmcnt(0)
	v_cvt_pk_bf16_f32 v86, v6, v7
	v_cvt_pk_bf16_f32 v87, v8, v9
	v_cvt_pk_bf16_f32 v88, v2, v3
	v_sub_co_u32_e32 v2, vcc, v96, v94
	v_cvt_pk_bf16_f32 v89, v4, v5
	v_sub_u32_e32 v8, 60, v92
	s_nop 0
	v_subb_co_u32_e32 v3, vcc, v97, v95, vcc
	global_load_dwordx4 v[2:5], v[2:3], off offset:240
	v_ashrrev_i32_e32 v9, 31, v8
	s_waitcnt vmcnt(0)
	v_pk_add_f32 v[4:5], v[46:47], v[4:5] op_sel:[0,1] op_sel_hi:[1,0]
	v_pk_add_f32 v[6:7], v[48:49], v[2:3] op_sel:[0,1] op_sel_hi:[1,0]
	v_lshlrev_b64 v[46:47], 2, v[8:9]
	s_nop 0
	v_mfma_f32_16x16x32_bf16 v[2:5], v[14:17], v[74:77], v[4:7]
	s_nop 2
	v_lshl_add_u64 v[6:7], v[90:91], 0, v[46:47]
	global_load_dwordx4 v[6:9], v[6:7], off
	v_mfma_f32_16x16x32_bf16 v[2:5], v[86:89], v[78:81], v[2:5]
	s_waitcnt vmcnt(0)
	v_pk_add_f32 v[8:9], v[42:43], v[8:9] op_sel:[0,1] op_sel_hi:[1,0]
	v_pk_add_f32 v[10:11], v[44:45], v[6:7] op_sel:[0,1] op_sel_hi:[1,0]
	s_nop 1
	v_mfma_f32_16x16x32_bf16 v[6:9], v[14:17], v[66:69], v[8:11]
	s_nop 2
	v_lshl_add_u64 v[10:11], v[110:111], 0, v[46:47]
	global_load_dwordx4 v[10:13], v[10:11], off
	v_mfma_f32_16x16x32_bf16 v[6:9], v[86:89], v[70:73], v[6:9]
	s_waitcnt vmcnt(0)
	v_pk_add_f32 v[38:39], v[38:39], v[12:13] op_sel:[0,1] op_sel_hi:[1,0]
	v_pk_add_f32 v[40:41], v[40:41], v[10:11] op_sel:[0,1] op_sel_hi:[1,0]
	s_nop 1
	v_mfma_f32_16x16x32_bf16 v[10:13], v[14:17], v[58:61], v[38:41]
	s_nop 2
	v_lshl_add_u64 v[38:39], v[112:113], 0, v[46:47]
	global_load_dwordx4 v[38:41], v[38:39], off
	v_mfma_f32_16x16x32_bf16 v[10:13], v[86:89], v[62:65], v[10:13]
	s_waitcnt vmcnt(0)
	v_pk_add_f32 v[34:35], v[34:35], v[40:41] op_sel:[0,1] op_sel_hi:[1,0]
	v_pk_add_f32 v[36:37], v[36:37], v[38:39] op_sel:[0,1] op_sel_hi:[1,0]
	v_mov_b32_e32 v38, v18
	v_mov_b32_e32 v39, v26
	v_mfma_f32_16x16x32_bf16 v[14:17], v[14:17], v[50:53], v[34:37]
	v_mov_b32_e32 v40, v22
	v_mov_b32_e32 v41, v30
	v_pk_add_f32 v[38:39], v[38:39], v[40:41]
	v_lshlrev_b64 v[34:35], 2, v[82:83]
	v_lshl_add_u64 v[36:37], s[16:17], 0, v[34:35]
	v_lshl_add_u64 v[34:35], s[18:19], 0, v[34:35]
	v_lshlrev_b32_e32 v82, 1, v100
	v_mfma_f32_16x16x32_bf16 v[14:17], v[86:89], v[54:57], v[14:17]
	global_load_dword v55, v[36:37], off
	global_load_dword v54, v[34:35], off
	global_load_dword v53, v[36:37], off offset:64
	global_load_dword v52, v[34:35], off offset:64
	global_load_dword v51, v[36:37], off offset:128
	global_load_dword v50, v[34:35], off offset:128
	global_load_dword v49, v[36:37], off offset:192
	global_load_dword v48, v[34:35], off offset:192
	v_add_u32_e32 v36, s4, v84
	v_lshl_add_u64 v[34:35], s[0:1], 0, v[82:83]
	s_movk_i32 s4, 0x1200
	v_mad_i64_i32 v[180:181], s[90:91], v36, s4, v[34:35]
	v_add_u32_e32 v196, 1, v36
	v_mad_i64_i32 v[182:183], s[90:91], v196, s4, v[34:35]
	v_add_u32_e32 v196, 2, v36
	v_mad_i64_i32 v[184:185], s[90:91], v196, s4, v[34:35]
	v_add_u32_e32 v196, 3, v36
	v_mad_i64_i32 v[186:187], s[90:91], v196, s4, v[34:35]
	v_add_u32_e32 v196, 16, v36
	v_mad_i64_i32 v[188:189], s[90:91], v196, s4, v[34:35]
	v_add_u32_e32 v196, 17, v36
	v_mad_i64_i32 v[190:191], s[90:91], v196, s4, v[34:35]
	v_add_u32_e32 v196, 18, v36
	v_mad_i64_i32 v[192:193], s[90:91], v196, s4, v[34:35]
	v_add_u32_e32 v196, 19, v36
	v_mad_i64_i32 v[194:195], s[90:91], v196, s4, v[34:35]
	global_load_ushort v114, v[180:181], off offset:1536
	global_load_ushort v115, v[180:181], off offset:2048
	global_load_ushort v116, v[180:181], off offset:1568
	global_load_ushort v117, v[180:181], off offset:2080
	global_load_ushort v118, v[180:181], off offset:1600
	global_load_ushort v119, v[180:181], off offset:2112
	global_load_ushort v120, v[180:181], off offset:1632
	global_load_ushort v121, v[180:181], off offset:2144
	global_load_ushort v122, v[182:183], off offset:1536
	global_load_ushort v123, v[182:183], off offset:2048
	global_load_ushort v124, v[182:183], off offset:1568
	global_load_ushort v125, v[182:183], off offset:2080
	global_load_ushort v126, v[182:183], off offset:1600
	global_load_ushort v127, v[182:183], off offset:2112
	global_load_ushort v128, v[182:183], off offset:1632
	global_load_ushort v129, v[182:183], off offset:2144
	global_load_ushort v130, v[184:185], off offset:1536
	global_load_ushort v131, v[184:185], off offset:2048
	global_load_ushort v132, v[184:185], off offset:1568
	global_load_ushort v133, v[184:185], off offset:2080
	global_load_ushort v134, v[184:185], off offset:1600
	global_load_ushort v135, v[184:185], off offset:2112
	global_load_ushort v136, v[184:185], off offset:1632
	global_load_ushort v137, v[184:185], off offset:2144
	global_load_ushort v138, v[186:187], off offset:1536
	global_load_ushort v139, v[186:187], off offset:2048
	global_load_ushort v140, v[186:187], off offset:1568
	global_load_ushort v141, v[186:187], off offset:2080
	global_load_ushort v142, v[186:187], off offset:1600
	global_load_ushort v143, v[186:187], off offset:2112
	global_load_ushort v144, v[186:187], off offset:1632
	global_load_ushort v145, v[186:187], off offset:2144
	global_load_ushort v146, v[188:189], off offset:1536
	global_load_ushort v147, v[188:189], off offset:2048
	global_load_ushort v148, v[188:189], off offset:1568
	global_load_ushort v149, v[188:189], off offset:2080
	global_load_ushort v150, v[188:189], off offset:1600
	global_load_ushort v151, v[188:189], off offset:2112
	global_load_ushort v152, v[188:189], off offset:1632
	global_load_ushort v153, v[188:189], off offset:2144
	global_load_ushort v155, v[190:191], off offset:1536
	global_load_ushort v156, v[190:191], off offset:2048
	global_load_ushort v157, v[190:191], off offset:1568
	global_load_ushort v158, v[190:191], off offset:2080
	global_load_ushort v159, v[190:191], off offset:1600
	global_load_ushort v160, v[190:191], off offset:2112
	global_load_ushort v161, v[190:191], off offset:1632
	global_load_ushort v162, v[190:191], off offset:2144
	global_load_ushort v163, v[192:193], off offset:1536
	global_load_ushort v164, v[192:193], off offset:2048
	global_load_ushort v165, v[192:193], off offset:1568
	global_load_ushort v166, v[192:193], off offset:2080
	global_load_ushort v167, v[192:193], off offset:1600
	global_load_ushort v168, v[192:193], off offset:2112
	global_load_ushort v169, v[192:193], off offset:1632
	global_load_ushort v170, v[192:193], off offset:2144
	global_load_ushort v171, v[194:195], off offset:2048
	global_load_ushort v172, v[194:195], off offset:1536
	global_load_ushort v173, v[194:195], off offset:1600
	global_load_ushort v174, v[194:195], off offset:1632
	global_load_ushort v175, v[194:195], off offset:1568
	global_load_ushort v176, v[194:195], off offset:2080
	global_load_ushort v177, v[194:195], off offset:2112
	global_load_ushort v178, v[194:195], off offset:2144
	v_mad_i64_i32 v[42:43], s[0:1], v36, s4, v[34:35]
	v_mov_b32_e32 v40, v18
	v_mov_b32_e32 v18, v114
	v_add_f32_e32 v37, v38, v39
	v_mov_b32_e32 v41, v22
	v_mov_b32_e32 v22, v19
	v_add_f32_dpp v37, v37, v37 quad_perm:[1,0,3,2] row_mask:0xf bank_mask:0xf bound_ctrl:1
	s_mov_b32 s0, 0x3a27c5ac
	v_readlane_b32 s18, v253, 13
	v_add_f32_dpp v37, v37, v37 quad_perm:[2,3,0,1] row_mask:0xf bank_mask:0xf bound_ctrl:1
	v_readlane_b32 s19, v253, 14
	s_mov_b64 s[16:17], 0x25bb0600
	v_add_f32_dpp v37, v37, v37 row_half_mirror row_mask:0xf bank_mask:0xf bound_ctrl:1
	s_waitcnt vmcnt(0)
	v_lshlrev_b32_e32 v61, 16, v18
	v_mov_b32_e32 v18, v115
	v_add_f32_dpp v37, v37, v37 row_mirror row_mask:0xf bank_mask:0xf bound_ctrl:1
	v_mul_f32_e32 v38, 0x3c800000, v37
	v_pk_add_f32 v[44:45], v[40:41], v[38:39] op_sel_hi:[1,0] neg_lo:[0,1] neg_hi:[0,1]
	v_mov_b32_e32 v40, v30
	v_mov_b32_e32 v41, v26
	v_ashrrev_i32_e32 v37, 31, v36
	v_pk_add_f32 v[38:39], v[40:41], v[38:39] op_sel_hi:[1,0] neg_lo:[0,1] neg_hi:[0,1]
	v_lshlrev_b64 v[40:41], 11, v[36:37]
	v_mov_b32_e32 v26, v19
	v_mov_b32_e32 v30, v23
	v_pk_mul_f32 v[64:65], v[44:45], v[44:45]
	v_pk_mul_f32 v[66:67], v[38:39], v[38:39]
	v_lshl_add_u64 v[40:41], s[18:19], 0, v[40:41]
	v_lshl_add_u64 v[40:41], v[40:41], 0, s[50:51]
	v_lshl_add_u64 v[46:47], v[40:41], 0, v[82:83]
	v_lshl_add_u64 v[40:41], v[46:47], 0, s[16:17]
	v_lshlrev_b32_e32 v62, 16, v18
	v_mov_b32_e32 v18, v116
	v_lshlrev_b32_e32 v59, 16, v18
	v_mov_b32_e32 v18, v117
	v_lshlrev_b32_e32 v60, 16, v18
	v_mov_b32_e32 v18, v118
	v_lshlrev_b32_e32 v57, 16, v18
	v_mov_b32_e32 v18, v119
	v_lshlrev_b32_e32 v58, 16, v18
	v_mov_b32_e32 v18, v120
	v_lshlrev_b32_e32 v37, 16, v18
	v_mov_b32_e32 v18, v121
	v_pk_add_f32 v[42:43], v[26:27], v[30:31]
	v_mov_b32_e32 v26, v31
	v_mov_b32_e32 v31, v64
	v_lshlrev_b32_e32 v56, 16, v18
	v_add_f32_e32 v18, v42, v43
	s_nop 1
	v_add_f32_dpp v18, v18, v18 quad_perm:[1,0,3,2] row_mask:0xf bank_mask:0xf bound_ctrl:1
	s_nop 1
	v_add_f32_dpp v18, v18, v18 quad_perm:[2,3,0,1] row_mask:0xf bank_mask:0xf bound_ctrl:1
	s_nop 1
	v_add_f32_dpp v18, v18, v18 row_half_mirror row_mask:0xf bank_mask:0xf bound_ctrl:1
	s_nop 1
	v_add_f32_dpp v18, v18, v18 row_mirror row_mask:0xf bank_mask:0xf bound_ctrl:1
	v_mul_f32_e32 v18, 0x3c800000, v18
	v_pk_add_f32 v[42:43], v[22:23], v[18:19] op_sel_hi:[1,0] neg_lo:[0,1] neg_hi:[0,1]
	v_pk_add_f32 v[22:23], v[26:27], v[18:19] op_sel_hi:[1,0] neg_lo:[0,1] neg_hi:[0,1]
	v_pk_mul_f32 v[68:69], v[42:43], v[42:43]
	v_pk_mul_f32 v[18:19], v[22:23], v[22:23]
	v_mov_b32_e32 v30, v68
	v_mov_b32_e32 v64, v69
	v_pk_add_f32 v[30:31], v[30:31], v[64:65]
	v_mov_b32_e32 v64, v19
	v_mov_b32_e32 v65, v67
	v_pk_add_f32 v[30:31], v[64:65], v[30:31]
	v_mov_b32_e32 v19, v66
	v_pk_add_f32 v[18:19], v[18:19], v[30:31]
	v_add_u32_e32 v26, 1, v36
	s_nop 0
	v_mov_b32_dpp v31, v19 quad_perm:[1,0,3,2] row_mask:0xf bank_mask:0xf bound_ctrl:1
	v_mov_b32_dpp v30, v18 quad_perm:[1,0,3,2] row_mask:0xf bank_mask:0xf bound_ctrl:1
	v_pk_add_f32 v[18:19], v[18:19], v[30:31]
	s_nop 1
	v_mov_b32_dpp v31, v19 quad_perm:[2,3,0,1] row_mask:0xf bank_mask:0xf bound_ctrl:1
	v_mov_b32_dpp v30, v18 quad_perm:[2,3,0,1] row_mask:0xf bank_mask:0xf bound_ctrl:1
	v_pk_add_f32 v[18:19], v[18:19], v[30:31]
	s_nop 1
	v_mov_b32_dpp v31, v19 row_half_mirror row_mask:0xf bank_mask:0xf bound_ctrl:1
	v_mov_b32_dpp v30, v18 row_half_mirror row_mask:0xf bank_mask:0xf bound_ctrl:1
	v_pk_add_f32 v[18:19], v[18:19], v[30:31]
	s_nop 1
	v_mov_b32_dpp v31, v19 row_mirror row_mask:0xf bank_mask:0xf bound_ctrl:1
	v_mov_b32_dpp v30, v18 row_mirror row_mask:0xf bank_mask:0xf bound_ctrl:1
	v_pk_add_f32 v[30:31], v[18:19], v[30:31]
	v_mov_b64_e32 v[18:19], s[0:1]
	v_pk_fma_f32 v[30:31], v[30:31], s[14:15], v[18:19] op_sel_hi:[1,0,0]
	s_nop 0
	v_mul_f32_e32 v27, 0x4b800000, v31
	v_cmp_gt_f32_e64 s[0:1], s64, v31
	v_cmp_gt_f32_e32 vcc, s64, v30
	s_nop 0
	v_cndmask_b32_e64 v27, v31, v27, s[0:1]
	v_rsq_f32_e32 v27, v27
	s_nop 0
	v_mul_f32_e32 v31, 0x45800000, v27
	v_cndmask_b32_e64 v27, v27, v31, s[0:1]
	v_mul_f32_e32 v31, v44, v27
	v_fma_f32 v31, v55, v31, v54
	v_add_f32_e32 v31, v31, v61
	v_mul_f32_e32 v31, v31, v62
	v_bfe_u32 v44, v31, 16, 1
	v_add_co_u32_e64 v46, s[0:1], s6, v46
	v_add3_u32 v31, v31, v44, s5
	s_nop 0
	v_addc_co_u32_e64 v47, s[0:1], 0, v47, s[0:1]
	global_store_short_d16_hi v[46:47], v31, off offset:1536
	v_mul_f32_e32 v31, v45, v27
	v_fma_f32 v31, v53, v31, v52
	v_add_f32_e32 v31, v31, v59
	v_mul_f32_e32 v31, v31, v60
	v_bfe_u32 v44, v31, 16, 1
	v_add3_u32 v31, v31, v44, s5
	global_store_short_d16_hi v[40:41], v31, off offset:32
	v_mul_f32_e32 v31, v39, v27
	v_fma_f32 v31, v51, v31, v50
	v_add_f32_e32 v31, v31, v57
	v_mul_f32_e32 v27, v38, v27
	v_mul_f32_e32 v31, v31, v58
	v_fma_f32 v27, v49, v27, v48
	v_bfe_u32 v39, v31, 16, 1
	v_add_f32_e32 v27, v27, v37
	v_add3_u32 v31, v31, v39, s5
	v_mul_f32_e32 v27, v27, v56
	global_store_short_d16_hi v[40:41], v31, off offset:64
	v_bfe_u32 v31, v27, 16, 1
	v_add3_u32 v27, v27, v31, s5
	global_store_short_d16_hi v[40:41], v27, off offset:96
	v_mul_f32_e32 v27, 0x4b800000, v30
	v_cndmask_b32_e32 v27, v30, v27, vcc
	v_rsq_f32_e32 v27, v27
	s_nop 0
	v_mul_f32_e32 v30, 0x45800000, v27
	v_cndmask_b32_e32 v37, v27, v30, vcc
	v_mad_i64_i32 v[30:31], s[0:1], v26, s4, v[34:35]
	v_mov_b32_e32 v41, v122
	v_mul_f32_e32 v40, v42, v37
	v_fma_f32 v40, v55, v40, v54
	v_ashrrev_i32_e32 v27, 31, v26
	v_lshlrev_b64 v[26:27], 11, v[26:27]
	v_lshl_add_u64 v[26:27], s[18:19], 0, v[26:27]
	v_lshl_add_u64 v[26:27], v[26:27], 0, s[50:51]
	v_lshl_add_u64 v[26:27], v[26:27], 0, v[82:83]
	v_lshl_add_u64 v[38:39], v[26:27], 0, s[16:17]
	v_add_co_u32_e32 v26, vcc, s6, v26
	v_mul_f32_e32 v23, v23, v37
	s_nop 0
	v_addc_co_u32_e32 v27, vcc, 0, v27, vcc
	v_fma_f32 v23, v51, v23, v50
	v_mul_f32_e32 v22, v22, v37
	v_fma_f32 v22, v49, v22, v48
	v_lshlrev_b32_e32 v41, 16, v41
	v_add_f32_e32 v40, v40, v41
	v_mov_b32_e32 v41, v123
	v_lshlrev_b32_e32 v41, 16, v41
	v_mul_f32_e32 v40, v40, v41
	v_bfe_u32 v41, v40, 16, 1
	v_add3_u32 v40, v40, v41, s5
	global_store_short_d16_hi v[26:27], v40, off offset:1536
	v_mov_b32_e32 v27, v124
	v_mul_f32_e32 v26, v43, v37
	v_fma_f32 v26, v53, v26, v52
	v_add_u32_e32 v40, 2, v36
	v_mad_i64_i32 v[42:43], s[0:1], v40, s4, v[34:35]
	v_ashrrev_i32_e32 v41, 31, v40
	v_lshlrev_b64 v[40:41], 11, v[40:41]
	v_lshl_add_u64 v[40:41], s[18:19], 0, v[40:41]
	v_lshl_add_u64 v[40:41], v[40:41], 0, s[50:51]
	v_lshl_add_u64 v[44:45], v[40:41], 0, v[82:83]
	v_lshl_add_u64 v[40:41], v[44:45], 0, s[16:17]
	v_lshlrev_b32_e32 v27, 16, v27
	v_add_f32_e32 v26, v26, v27
	v_mov_b32_e32 v27, v125
	v_lshlrev_b32_e32 v27, 16, v27
	v_mul_f32_e32 v26, v26, v27
	v_bfe_u32 v27, v26, 16, 1
	v_add3_u32 v26, v26, v27, s5
	global_store_short_d16_hi v[38:39], v26, off offset:32
	v_mov_b32_e32 v26, v126
	v_mov_b32_e32 v27, v32
	v_lshlrev_b32_e32 v26, 16, v26
	v_add_f32_e32 v23, v23, v26
	v_mov_b32_e32 v26, v127
	v_lshlrev_b32_e32 v26, 16, v26
	v_mul_f32_e32 v23, v23, v26
	v_bfe_u32 v26, v23, 16, 1
	v_add3_u32 v23, v23, v26, s5
	global_store_short_d16_hi v[38:39], v23, off offset:64
	v_mov_b32_e32 v23, v128
	v_mov_b32_e32 v26, v24
	v_lshlrev_b32_e32 v23, 16, v23
	v_add_f32_e32 v22, v22, v23
	v_mov_b32_e32 v23, v129
	v_mov_b32_e32 v30, v32
	v_mov_b32_e32 v31, v28
	v_mov_b32_e32 v32, v25
	v_lshlrev_b32_e32 v23, 16, v23
	v_mul_f32_e32 v22, v22, v23
	v_bfe_u32 v23, v22, 16, 1
	v_add3_u32 v22, v22, v23, s5
	global_store_short_d16_hi v[38:39], v22, off offset:96
	v_mov_b32_e32 v22, v20
	v_mov_b32_e32 v23, v28
	v_pk_add_f32 v[22:23], v[22:23], v[26:27]
	v_mov_b32_e32 v26, v20
	v_mov_b32_e32 v20, v130
	v_mov_b32_e32 v28, v21
	v_add_f32_e32 v22, v22, v23
	v_mov_b32_e32 v27, v24
	v_mov_b32_e32 v24, v21
	v_add_f32_dpp v22, v22, v22 quad_perm:[1,0,3,2] row_mask:0xf bank_mask:0xf bound_ctrl:1
	v_lshlrev_b32_e32 v37, 16, v20
	v_mov_b32_e32 v20, v131
	v_add_f32_dpp v22, v22, v22 quad_perm:[2,3,0,1] row_mask:0xf bank_mask:0xf bound_ctrl:1
	v_lshlrev_b32_e32 v56, 16, v20
	v_mov_b32_e32 v20, v132
	v_add_f32_dpp v22, v22, v22 row_half_mirror row_mask:0xf bank_mask:0xf bound_ctrl:1
	v_lshlrev_b32_e32 v57, 16, v20
	v_mov_b32_e32 v20, v133
	v_add_f32_dpp v22, v22, v22 row_mirror row_mask:0xf bank_mask:0xf bound_ctrl:1
	v_mul_f32_e32 v22, 0x3c800000, v22
	v_pk_add_f32 v[26:27], v[26:27], v[22:23] op_sel_hi:[1,0] neg_lo:[0,1] neg_hi:[0,1]
	v_pk_add_f32 v[22:23], v[30:31], v[22:23] op_sel_hi:[1,0] neg_lo:[0,1] neg_hi:[0,1]
	v_pk_mul_f32 v[38:39], v[26:27], v[26:27]
	v_pk_mul_f32 v[30:31], v[22:23], v[22:23]
	v_mov_b32_e32 v47, v38
	v_lshlrev_b32_e32 v58, 16, v20
	v_mov_b32_e32 v20, v134
	v_lshlrev_b32_e32 v59, 16, v20
	v_mov_b32_e32 v20, v135
	v_lshlrev_b32_e32 v60, 16, v20
	v_mov_b32_e32 v20, v136
	v_lshlrev_b32_e32 v61, 16, v20
	v_mov_b32_e32 v20, v137
	v_pk_add_f32 v[42:43], v[28:29], v[32:33]
	v_mov_b32_e32 v28, v33
	v_add_u32_e32 v32, 3, v36
	v_ashrrev_i32_e32 v33, 31, v32
	v_lshlrev_b32_e32 v62, 16, v20
	v_add_f32_e32 v20, v42, v43
	s_nop 1
	v_add_f32_dpp v20, v20, v20 quad_perm:[1,0,3,2] row_mask:0xf bank_mask:0xf bound_ctrl:1
	s_nop 1
	v_add_f32_dpp v20, v20, v20 quad_perm:[2,3,0,1] row_mask:0xf bank_mask:0xf bound_ctrl:1
	s_nop 1
	v_add_f32_dpp v20, v20, v20 row_half_mirror row_mask:0xf bank_mask:0xf bound_ctrl:1
	s_nop 1
	v_add_f32_dpp v20, v20, v20 row_mirror row_mask:0xf bank_mask:0xf bound_ctrl:1
	v_mul_f32_e32 v20, 0x3c800000, v20
	v_pk_add_f32 v[24:25], v[24:25], v[20:21] op_sel_hi:[1,0] neg_lo:[0,1] neg_hi:[0,1]
	v_pk_add_f32 v[20:21], v[28:29], v[20:21] op_sel_hi:[1,0] neg_lo:[0,1] neg_hi:[0,1]
	v_pk_mul_f32 v[42:43], v[24:25], v[24:25]
	v_pk_mul_f32 v[28:29], v[20:21], v[20:21]
	v_mov_b32_e32 v46, v42
	v_mov_b32_e32 v38, v43
	v_pk_add_f32 v[38:39], v[46:47], v[38:39]
	v_mov_b32_e32 v42, v29
	v_mov_b32_e32 v43, v31
	v_pk_add_f32 v[38:39], v[42:43], v[38:39]
	v_mov_b32_e32 v29, v30
	v_pk_add_f32 v[28:29], v[28:29], v[38:39]
	s_nop 1
	v_mov_b32_dpp v31, v29 quad_perm:[1,0,3,2] row_mask:0xf bank_mask:0xf bound_ctrl:1
	v_mov_b32_dpp v30, v28 quad_perm:[1,0,3,2] row_mask:0xf bank_mask:0xf bound_ctrl:1
	v_pk_add_f32 v[28:29], v[28:29], v[30:31]
	s_nop 1
	v_mov_b32_dpp v31, v29 quad_perm:[2,3,0,1] row_mask:0xf bank_mask:0xf bound_ctrl:1
	v_mov_b32_dpp v30, v28 quad_perm:[2,3,0,1] row_mask:0xf bank_mask:0xf bound_ctrl:1
	v_pk_add_f32 v[28:29], v[28:29], v[30:31]
	s_nop 1
	v_mov_b32_dpp v31, v29 row_half_mirror row_mask:0xf bank_mask:0xf bound_ctrl:1
	v_mov_b32_dpp v30, v28 row_half_mirror row_mask:0xf bank_mask:0xf bound_ctrl:1
	v_pk_add_f32 v[28:29], v[28:29], v[30:31]
	s_nop 1
	v_mov_b32_dpp v31, v29 row_mirror row_mask:0xf bank_mask:0xf bound_ctrl:1
	v_mov_b32_dpp v30, v28 row_mirror row_mask:0xf bank_mask:0xf bound_ctrl:1
	v_pk_add_f32 v[28:29], v[28:29], v[30:31]
	s_nop 0
	v_pk_fma_f32 v[28:29], v[28:29], s[14:15], v[18:19] op_sel_hi:[1,0,0]
	s_nop 0
	v_mul_f32_e32 v30, 0x4b800000, v29
	v_cmp_gt_f32_e64 s[0:1], s64, v29
	v_cmp_gt_f32_e32 vcc, s64, v28
	s_nop 0
	v_cndmask_b32_e64 v29, v29, v30, s[0:1]
	v_rsq_f32_e32 v29, v29
	s_nop 0
	v_mul_f32_e32 v30, 0x45800000, v29
	v_cndmask_b32_e64 v29, v29, v30, s[0:1]
	v_mul_f32_e32 v26, v26, v29
	v_fma_f32 v26, v55, v26, v54
	v_add_f32_e32 v26, v26, v37
	v_mul_f32_e32 v26, v26, v56
	v_bfe_u32 v30, v26, 16, 1
	v_add3_u32 v26, v26, v30, s5
	v_add_co_u32_e64 v30, s[0:1], s6, v44
	v_mul_f32_e32 v23, v23, v29
	s_nop 0
	v_addc_co_u32_e64 v31, s[0:1], 0, v45, s[0:1]
	global_store_short_d16_hi v[30:31], v26, off offset:1536
	v_mul_f32_e32 v26, v27, v29
	v_fma_f32 v26, v53, v26, v52
	v_add_f32_e32 v26, v26, v57
	v_mul_f32_e32 v26, v26, v58
	v_fma_f32 v23, v51, v23, v50
	v_bfe_u32 v27, v26, 16, 1
	v_add_f32_e32 v23, v23, v59
	v_mul_f32_e32 v22, v22, v29
	v_add3_u32 v26, v26, v27, s5
	v_mul_f32_e32 v23, v23, v60
	v_fma_f32 v22, v49, v22, v48
	global_store_short_d16_hi v[40:41], v26, off offset:32
	v_bfe_u32 v26, v23, 16, 1
	v_add_f32_e32 v22, v22, v61
	v_add3_u32 v23, v23, v26, s5
	v_mul_f32_e32 v22, v22, v62
	global_store_short_d16_hi v[40:41], v23, off offset:64
	v_bfe_u32 v23, v22, 16, 1
	v_add3_u32 v22, v22, v23, s5
	global_store_short_d16_hi v[40:41], v22, off offset:96
	v_mul_f32_e32 v22, 0x4b800000, v28
	v_cndmask_b32_e32 v22, v28, v22, vcc
	v_rsq_f32_e32 v22, v22
	v_lshlrev_b64 v[26:27], 11, v[32:33]
	v_lshl_add_u64 v[26:27], s[18:19], 0, v[26:27]
	v_lshl_add_u64 v[26:27], v[26:27], 0, s[50:51]
	v_mul_f32_e32 v23, 0x45800000, v22
	v_cndmask_b32_e32 v30, v22, v23, vcc
	v_mad_i64_i32 v[22:23], s[0:1], v32, s4, v[34:35]
	v_mov_b32_e32 v31, v138
	v_mul_f32_e32 v24, v24, v30
	v_fma_f32 v24, v55, v24, v54
	v_lshl_add_u64 v[26:27], v[26:27], 0, v[82:83]
	v_lshl_add_u64 v[28:29], v[26:27], 0, s[16:17]
	v_add_co_u32_e32 v26, vcc, s6, v26
	v_mul_f32_e32 v21, v21, v30
	s_nop 0
	v_addc_co_u32_e32 v27, vcc, 0, v27, vcc
	v_fma_f32 v21, v51, v21, v50
	v_mul_f32_e32 v20, v20, v30
	v_fma_f32 v20, v49, v20, v48
	v_lshlrev_b32_e32 v31, 16, v31
	v_add_f32_e32 v24, v24, v31
	v_mov_b32_e32 v31, v139
	v_lshlrev_b32_e32 v31, 16, v31
	v_mul_f32_e32 v24, v24, v31
	v_bfe_u32 v31, v24, 16, 1
	v_add3_u32 v24, v24, v31, s5
	global_store_short_d16_hi v[26:27], v24, off offset:1536
	v_mul_f32_e32 v24, v25, v30
	v_mov_b32_e32 v25, v140
	v_fma_f32 v24, v53, v24, v52
	v_mov_b32_e32 v26, v14
	v_mov_b32_e32 v27, v10
	v_lshlrev_b32_e32 v25, 16, v25
	v_add_f32_e32 v24, v24, v25
	v_mov_b32_e32 v25, v141
	v_lshlrev_b32_e32 v25, 16, v25
	v_mul_f32_e32 v24, v24, v25
	v_bfe_u32 v25, v24, 16, 1
	v_add3_u32 v24, v24, v25, s5
	global_store_short_d16_hi v[28:29], v24, off offset:32
	v_mov_b32_e32 v24, v142
	v_mov_b32_e32 v25, v14
	v_mov_b32_e32 v14, v7
	v_lshlrev_b32_e32 v24, 16, v24
	v_add_f32_e32 v21, v21, v24
	v_mov_b32_e32 v24, v143
	v_lshlrev_b32_e32 v24, 16, v24
	v_mul_f32_e32 v21, v21, v24
	v_bfe_u32 v24, v21, 16, 1
	v_add3_u32 v21, v21, v24, s5
	global_store_short_d16_hi v[28:29], v21, off offset:64
	v_mov_b32_e32 v21, v144
	v_mov_b32_e32 v24, v6
	v_lshlrev_b32_e32 v21, 16, v21
	v_add_f32_e32 v20, v20, v21
	v_mov_b32_e32 v21, v145
	v_add_u32_e32 v22, 16, v36
	v_mad_i64_i32 v[32:33], s[0:1], v22, s4, v[34:35]
	v_ashrrev_i32_e32 v23, 31, v22
	v_lshlrev_b64 v[22:23], 11, v[22:23]
	v_lshl_add_u64 v[22:23], s[18:19], 0, v[22:23]
	v_lshl_add_u64 v[22:23], v[22:23], 0, s[50:51]
	v_lshlrev_b32_e32 v21, 16, v21
	v_mul_f32_e32 v20, v20, v21
	v_bfe_u32 v21, v20, 16, 1
	v_add3_u32 v20, v20, v21, s5
	global_store_short_d16_hi v[28:29], v20, off offset:96
	v_mov_b32_e32 v20, v2
	v_mov_b32_e32 v21, v10
	v_pk_add_f32 v[20:21], v[20:21], v[24:25]
	v_mov_b32_e32 v24, v2
	v_mov_b32_e32 v2, v146
	v_mov_b32_e32 v10, v3
	v_add_f32_e32 v20, v20, v21
	v_mov_b32_e32 v25, v6
	v_mov_b32_e32 v6, v3
	v_add_f32_dpp v20, v20, v20 quad_perm:[1,0,3,2] row_mask:0xf bank_mask:0xf bound_ctrl:1
	v_lshlrev_b32_e32 v37, 16, v2
	v_mov_b32_e32 v2, v147
	v_add_f32_dpp v20, v20, v20 quad_perm:[2,3,0,1] row_mask:0xf bank_mask:0xf bound_ctrl:1
	v_lshlrev_b32_e32 v40, 16, v2
	v_mov_b32_e32 v2, v148
	v_add_f32_dpp v20, v20, v20 row_half_mirror row_mask:0xf bank_mask:0xf bound_ctrl:1
	v_lshlrev_b32_e32 v41, 16, v2
	v_mov_b32_e32 v2, v149
	v_add_f32_dpp v20, v20, v20 row_mirror row_mask:0xf bank_mask:0xf bound_ctrl:1
	v_mul_f32_e32 v20, 0x3c800000, v20
	v_pk_add_f32 v[24:25], v[24:25], v[20:21] op_sel_hi:[1,0] neg_lo:[0,1] neg_hi:[0,1]
	v_pk_add_f32 v[20:21], v[26:27], v[20:21] op_sel_hi:[1,0] neg_lo:[0,1] neg_hi:[0,1]
	v_pk_mul_f32 v[30:31], v[24:25], v[24:25]
	v_pk_mul_f32 v[28:29], v[20:21], v[20:21]
	v_mov_b32_e32 v39, v30
	v_lshl_add_u64 v[26:27], v[22:23], 0, v[82:83]
	v_lshl_add_u64 v[22:23], v[26:27], 0, s[16:17]
	v_lshlrev_b32_e32 v42, 16, v2
	v_mov_b32_e32 v2, v150
	v_lshlrev_b32_e32 v43, 16, v2
	v_mov_b32_e32 v2, v151
	v_lshlrev_b32_e32 v44, 16, v2
	v_mov_b32_e32 v2, v152
	v_lshlrev_b32_e32 v45, 16, v2
	v_mov_b32_e32 v2, v153
	v_pk_add_f32 v[32:33], v[10:11], v[14:15]
	v_mov_b32_e32 v10, v15
	v_add_u32_e32 v14, 17, v36
	v_lshlrev_b32_e32 v46, 16, v2
	v_add_f32_e32 v2, v32, v33
	s_nop 1
	v_add_f32_dpp v2, v2, v2 quad_perm:[1,0,3,2] row_mask:0xf bank_mask:0xf bound_ctrl:1
	s_nop 1
	v_add_f32_dpp v2, v2, v2 quad_perm:[2,3,0,1] row_mask:0xf bank_mask:0xf bound_ctrl:1
	s_nop 1
	v_add_f32_dpp v2, v2, v2 row_half_mirror row_mask:0xf bank_mask:0xf bound_ctrl:1
	s_nop 1
	v_add_f32_dpp v2, v2, v2 row_mirror row_mask:0xf bank_mask:0xf bound_ctrl:1
	v_mul_f32_e32 v2, 0x3c800000, v2
	v_pk_add_f32 v[6:7], v[6:7], v[2:3] op_sel_hi:[1,0] neg_lo:[0,1] neg_hi:[0,1]
	v_pk_add_f32 v[2:3], v[10:11], v[2:3] op_sel_hi:[1,0] neg_lo:[0,1] neg_hi:[0,1]
	v_pk_mul_f32 v[32:33], v[6:7], v[6:7]
	v_pk_mul_f32 v[10:11], v[2:3], v[2:3]
	v_mov_b32_e32 v38, v32
	v_mov_b32_e32 v30, v33
	v_pk_add_f32 v[30:31], v[38:39], v[30:31]
	v_mov_b32_e32 v32, v11
	v_mov_b32_e32 v33, v29
	v_pk_add_f32 v[30:31], v[32:33], v[30:31]
	v_mov_b32_e32 v11, v28
	v_pk_add_f32 v[10:11], v[10:11], v[30:31]
	s_nop 1
	v_mov_b32_dpp v29, v11 quad_perm:[1,0,3,2] row_mask:0xf bank_mask:0xf bound_ctrl:1
	v_mov_b32_dpp v28, v10 quad_perm:[1,0,3,2] row_mask:0xf bank_mask:0xf bound_ctrl:1
	v_pk_add_f32 v[10:11], v[10:11], v[28:29]
	s_nop 1
	v_mov_b32_dpp v29, v11 quad_perm:[2,3,0,1] row_mask:0xf bank_mask:0xf bound_ctrl:1
	v_mov_b32_dpp v28, v10 quad_perm:[2,3,0,1] row_mask:0xf bank_mask:0xf bound_ctrl:1
	v_pk_add_f32 v[10:11], v[10:11], v[28:29]
	s_nop 1
	v_mov_b32_dpp v29, v11 row_half_mirror row_mask:0xf bank_mask:0xf bound_ctrl:1
	v_mov_b32_dpp v28, v10 row_half_mirror row_mask:0xf bank_mask:0xf bound_ctrl:1
	v_pk_add_f32 v[10:11], v[10:11], v[28:29]
	s_nop 1
	v_mov_b32_dpp v29, v11 row_mirror row_mask:0xf bank_mask:0xf bound_ctrl:1
	v_mov_b32_dpp v28, v10 row_mirror row_mask:0xf bank_mask:0xf bound_ctrl:1
	v_pk_add_f32 v[10:11], v[10:11], v[28:29]
	s_nop 0
	v_pk_fma_f32 v[10:11], v[10:11], s[14:15], v[18:19] op_sel_hi:[1,0,0]
	s_nop 0
	v_mul_f32_e32 v15, 0x4b800000, v11
	v_cmp_gt_f32_e64 s[0:1], s64, v11
	v_cmp_gt_f32_e32 vcc, s64, v10
	s_nop 0
	v_cndmask_b32_e64 v11, v11, v15, s[0:1]
	v_rsq_f32_e32 v11, v11
	s_nop 0
	v_mul_f32_e32 v15, 0x45800000, v11
	v_cndmask_b32_e64 v11, v11, v15, s[0:1]
	v_mul_f32_e32 v15, v24, v11
	v_fma_f32 v15, v55, v15, v54
	v_add_f32_e32 v15, v15, v37
	v_mul_f32_e32 v15, v15, v40
	v_bfe_u32 v24, v15, 16, 1
	v_add_co_u32_e64 v26, s[0:1], s6, v26
	v_add3_u32 v15, v15, v24, s5
	s_nop 0
	v_addc_co_u32_e64 v27, s[0:1], 0, v27, s[0:1]
	global_store_short_d16_hi v[26:27], v15, off offset:1536
	v_mul_f32_e32 v15, v25, v11
	v_fma_f32 v15, v53, v15, v52
	v_add_f32_e32 v15, v15, v41
	v_mul_f32_e32 v15, v15, v42
	v_bfe_u32 v24, v15, 16, 1
	v_add3_u32 v15, v15, v24, s5
	global_store_short_d16_hi v[22:23], v15, off offset:32
	v_mul_f32_e32 v15, v21, v11
	v_fma_f32 v15, v51, v15, v50
	v_add_f32_e32 v15, v15, v43
	v_mul_f32_e32 v11, v20, v11
	v_mul_f32_e32 v15, v15, v44
	v_fma_f32 v11, v49, v11, v48
	v_bfe_u32 v21, v15, 16, 1
	v_add_f32_e32 v11, v11, v45
	v_add3_u32 v15, v15, v21, s5
	v_mul_f32_e32 v11, v11, v46
	global_store_short_d16_hi v[22:23], v15, off offset:64
	v_bfe_u32 v15, v11, 16, 1
	v_add3_u32 v11, v11, v15, s5
	global_store_short_d16_hi v[22:23], v11, off offset:96
	v_mul_f32_e32 v11, 0x4b800000, v10
	v_cndmask_b32_e32 v10, v10, v11, vcc
	v_rsq_f32_e32 v10, v10
	v_ashrrev_i32_e32 v15, 31, v14
	v_mul_f32_e32 v11, 0x45800000, v10
	v_cndmask_b32_e32 v22, v10, v11, vcc
	v_mad_i64_i32 v[10:11], s[0:1], v14, s4, v[34:35]
	v_mov_b32_e32 v23, v155
	v_mul_f32_e32 v6, v6, v22
	v_fma_f32 v6, v55, v6, v54
	v_lshlrev_b64 v[14:15], 11, v[14:15]
	v_lshl_add_u64 v[14:15], s[18:19], 0, v[14:15]
	v_lshl_add_u64 v[14:15], v[14:15], 0, s[50:51]
	v_lshl_add_u64 v[14:15], v[14:15], 0, v[82:83]
	v_lshl_add_u64 v[20:21], v[14:15], 0, s[16:17]
	v_add_co_u32_e32 v14, vcc, s6, v14
	v_mul_f32_e32 v3, v3, v22
	s_nop 0
	v_addc_co_u32_e32 v15, vcc, 0, v15, vcc
	v_fma_f32 v3, v51, v3, v50
	v_mul_f32_e32 v2, v2, v22
	v_fma_f32 v2, v49, v2, v48
	v_lshlrev_b32_e32 v23, 16, v23
	v_add_f32_e32 v6, v6, v23
	v_mov_b32_e32 v23, v156
	v_lshlrev_b32_e32 v23, 16, v23
	v_mul_f32_e32 v6, v6, v23
	v_bfe_u32 v23, v6, 16, 1
	v_add3_u32 v6, v6, v23, s5
	global_store_short_d16_hi v[14:15], v6, off offset:1536
	v_mul_f32_e32 v6, v7, v22
	v_mov_b32_e32 v7, v157
	v_fma_f32 v6, v53, v6, v52
	v_lshlrev_b32_e32 v7, 16, v7
	v_add_f32_e32 v6, v6, v7
	v_mov_b32_e32 v7, v158
	v_lshlrev_b32_e32 v7, 16, v7
	v_mul_f32_e32 v6, v6, v7
	v_bfe_u32 v7, v6, 16, 1
	v_add3_u32 v6, v6, v7, s5
	global_store_short_d16_hi v[20:21], v6, off offset:32
	v_mov_b32_e32 v6, v159
	v_mov_b32_e32 v7, v16
	v_lshlrev_b32_e32 v6, 16, v6
	v_add_f32_e32 v3, v3, v6
	v_mov_b32_e32 v6, v160
	v_lshlrev_b32_e32 v6, 16, v6
	v_mul_f32_e32 v3, v3, v6
	v_bfe_u32 v6, v3, 16, 1
	v_add3_u32 v3, v3, v6, s5
	global_store_short_d16_hi v[20:21], v3, off offset:64
	v_mov_b32_e32 v3, v161
	v_mov_b32_e32 v6, v8
	v_lshlrev_b32_e32 v3, 16, v3
	v_add_f32_e32 v2, v2, v3
	v_mov_b32_e32 v3, v162
	v_mov_b32_e32 v10, v16
	v_mov_b32_e32 v11, v12
	v_mov_b32_e32 v16, v9
	v_lshlrev_b32_e32 v3, 16, v3
	v_mul_f32_e32 v2, v2, v3
	v_bfe_u32 v3, v2, 16, 1
	v_add3_u32 v2, v2, v3, s5
	global_store_short_d16_hi v[20:21], v2, off offset:96
	v_add_u32_e32 v20, 18, v36
	v_mov_b32_e32 v2, v4
	v_mov_b32_e32 v3, v12
	v_mad_i64_i32 v[24:25], s[0:1], v20, s4, v[34:35]
	v_pk_add_f32 v[2:3], v[2:3], v[6:7]
	v_mov_b32_e32 v6, v4
	v_mov_b32_e32 v4, v163
	v_mov_b32_e32 v12, v5
	v_pk_add_f32 v[38:39], v[12:13], v[16:17]
	v_add_f32_e32 v2, v2, v3
	v_mov_b32_e32 v7, v8
	v_mov_b32_e32 v8, v5
	v_add_f32_dpp v2, v2, v2 quad_perm:[1,0,3,2] row_mask:0xf bank_mask:0xf bound_ctrl:1
	v_mov_b32_e32 v12, v17
	v_ashrrev_i32_e32 v21, 31, v20
	v_add_f32_dpp v2, v2, v2 quad_perm:[2,3,0,1] row_mask:0xf bank_mask:0xf bound_ctrl:1
	v_lshlrev_b64 v[20:21], 11, v[20:21]
	v_lshl_add_u64 v[20:21], s[18:19], 0, v[20:21]
	v_add_f32_dpp v2, v2, v2 row_half_mirror row_mask:0xf bank_mask:0xf bound_ctrl:1
	v_lshl_add_u64 v[20:21], v[20:21], 0, s[50:51]
	v_lshl_add_u64 v[22:23], v[20:21], 0, v[82:83]
	v_add_f32_dpp v2, v2, v2 row_mirror row_mask:0xf bank_mask:0xf bound_ctrl:1
	v_mul_f32_e32 v2, 0x3c800000, v2
	v_pk_add_f32 v[6:7], v[6:7], v[2:3] op_sel_hi:[1,0] neg_lo:[0,1] neg_hi:[0,1]
	v_pk_add_f32 v[2:3], v[10:11], v[2:3] op_sel_hi:[1,0] neg_lo:[0,1] neg_hi:[0,1]
	v_pk_mul_f32 v[14:15], v[6:7], v[6:7]
	v_pk_mul_f32 v[10:11], v[2:3], v[2:3]
	v_mov_b32_e32 v37, v14
	v_lshl_add_u64 v[20:21], v[22:23], 0, s[16:17]
	v_lshlrev_b32_e32 v26, 16, v4
	v_mov_b32_e32 v4, v164
	v_lshlrev_b32_e32 v28, 16, v4
	v_mov_b32_e32 v4, v165
	v_lshlrev_b32_e32 v27, 16, v4
	v_mov_b32_e32 v4, v166
	v_lshlrev_b32_e32 v29, 16, v4
	v_mov_b32_e32 v4, v167
	v_lshlrev_b32_e32 v30, 16, v4
	v_mov_b32_e32 v4, v168
	v_lshlrev_b32_e32 v32, 16, v4
	v_mov_b32_e32 v4, v169
	v_lshlrev_b32_e32 v31, 16, v4
	v_mov_b32_e32 v4, v170
	v_lshlrev_b32_e32 v24, 16, v4
	v_add_f32_e32 v4, v38, v39
	s_nop 1
	v_add_f32_dpp v4, v4, v4 quad_perm:[1,0,3,2] row_mask:0xf bank_mask:0xf bound_ctrl:1
	s_nop 1
	v_add_f32_dpp v4, v4, v4 quad_perm:[2,3,0,1] row_mask:0xf bank_mask:0xf bound_ctrl:1
	s_nop 1
	v_add_f32_dpp v4, v4, v4 row_half_mirror row_mask:0xf bank_mask:0xf bound_ctrl:1
	s_nop 1
	v_add_f32_dpp v4, v4, v4 row_mirror row_mask:0xf bank_mask:0xf bound_ctrl:1
	v_mul_f32_e32 v4, 0x3c800000, v4
	v_pk_add_f32 v[8:9], v[8:9], v[4:5] op_sel_hi:[1,0] neg_lo:[0,1] neg_hi:[0,1]
	v_pk_add_f32 v[4:5], v[12:13], v[4:5] op_sel_hi:[1,0] neg_lo:[0,1] neg_hi:[0,1]
	v_pk_mul_f32 v[38:39], v[8:9], v[8:9]
	v_pk_mul_f32 v[16:17], v[4:5], v[4:5]
	v_add_u32_e32 v12, 19, v36
	v_mov_b32_e32 v36, v38
	v_mov_b32_e32 v14, v39
	v_pk_add_f32 v[14:15], v[36:37], v[14:15]
	v_mov_b32_e32 v36, v17
	v_mov_b32_e32 v37, v11
	v_pk_add_f32 v[14:15], v[36:37], v[14:15]
	v_mov_b32_e32 v17, v10
	v_pk_add_f32 v[10:11], v[16:17], v[14:15]
	s_nop 1
	v_mov_b32_dpp v15, v11 quad_perm:[1,0,3,2] row_mask:0xf bank_mask:0xf bound_ctrl:1
	v_mov_b32_dpp v14, v10 quad_perm:[1,0,3,2] row_mask:0xf bank_mask:0xf bound_ctrl:1
	v_pk_add_f32 v[10:11], v[10:11], v[14:15]
	s_nop 1
	v_mov_b32_dpp v15, v11 quad_perm:[2,3,0,1] row_mask:0xf bank_mask:0xf bound_ctrl:1
	v_mov_b32_dpp v14, v10 quad_perm:[2,3,0,1] row_mask:0xf bank_mask:0xf bound_ctrl:1
	v_pk_add_f32 v[10:11], v[10:11], v[14:15]
	s_nop 1
	v_mov_b32_dpp v15, v11 row_half_mirror row_mask:0xf bank_mask:0xf bound_ctrl:1
	v_mov_b32_dpp v14, v10 row_half_mirror row_mask:0xf bank_mask:0xf bound_ctrl:1
	v_pk_add_f32 v[10:11], v[10:11], v[14:15]
	s_nop 1
	v_mov_b32_dpp v15, v11 row_mirror row_mask:0xf bank_mask:0xf bound_ctrl:1
	v_mov_b32_dpp v14, v10 row_mirror row_mask:0xf bank_mask:0xf bound_ctrl:1
	v_pk_add_f32 v[10:11], v[10:11], v[14:15]
	s_nop 0
	v_pk_fma_f32 v[10:11], v[10:11], s[14:15], v[18:19] op_sel_hi:[1,0,0]
	s_nop 0
	v_mul_f32_e32 v13, 0x4b800000, v11
	v_cmp_gt_f32_e64 s[0:1], s64, v11
	v_cmp_gt_f32_e32 vcc, s64, v10
	s_nop 0
	v_cndmask_b32_e64 v11, v11, v13, s[0:1]
	v_rsq_f32_e32 v11, v11
	s_nop 0
	v_mul_f32_e32 v13, 0x45800000, v11
	v_cndmask_b32_e64 v11, v11, v13, s[0:1]
	v_mul_f32_e32 v6, v6, v11
	v_fma_f32 v6, v55, v6, v54
	v_add_f32_e32 v6, v6, v26
	v_mul_f32_e32 v6, v6, v28
	v_bfe_u32 v13, v6, 16, 1
	v_add_co_u32_e64 v14, s[0:1], s6, v22
	v_add3_u32 v6, v6, v13, s5
	s_nop 0
	v_addc_co_u32_e64 v15, s[0:1], 0, v23, s[0:1]
	global_store_short_d16_hi v[14:15], v6, off offset:1536
	v_mul_f32_e32 v6, v7, v11
	v_fma_f32 v6, v53, v6, v52
	v_add_f32_e32 v6, v6, v27
	v_mul_f32_e32 v3, v3, v11
	v_mul_f32_e32 v6, v6, v29
	v_fma_f32 v3, v51, v3, v50
	v_bfe_u32 v7, v6, 16, 1
	v_add_f32_e32 v3, v3, v30
	v_mul_f32_e32 v2, v2, v11
	v_add3_u32 v6, v6, v7, s5
	v_mul_f32_e32 v3, v3, v32
	v_fma_f32 v2, v49, v2, v48
	global_store_short_d16_hi v[20:21], v6, off offset:32
	v_bfe_u32 v6, v3, 16, 1
	v_add_f32_e32 v2, v2, v31
	v_add3_u32 v3, v3, v6, s5
	v_mul_f32_e32 v2, v2, v24
	global_store_short_d16_hi v[20:21], v3, off offset:64
	v_bfe_u32 v3, v2, 16, 1
	v_add3_u32 v2, v2, v3, s5
	global_store_short_d16_hi v[20:21], v2, off offset:96
	v_mul_f32_e32 v2, 0x4b800000, v10
	v_cndmask_b32_e32 v2, v10, v2, vcc
	v_rsq_f32_e32 v2, v2
	v_mad_i64_i32 v[6:7], s[0:1], v12, s4, v[34:35]
	v_mov_b32_e32 v11, v171
	v_mul_f32_e32 v3, 0x45800000, v2
	v_cndmask_b32_e32 v10, v2, v3, vcc
	v_mul_f32_e32 v8, v8, v10
	v_fmac_f32_e32 v54, v55, v8
	v_mov_b32_e32 v8, v172
	v_ashrrev_i32_e32 v13, 31, v12
	v_lshlrev_b64 v[2:3], 11, v[12:13]
	v_mul_f32_e32 v5, v5, v10
	v_lshl_add_u64 v[2:3], s[18:19], 0, v[2:3]
	v_fmac_f32_e32 v50, v51, v5
	v_mov_b32_e32 v5, v173
	v_lshl_add_u64 v[2:3], v[2:3], 0, s[50:51]
	v_lshl_add_u64 v[12:13], v[2:3], 0, v[82:83]
	v_lshl_add_u64 v[2:3], v[12:13], 0, s[16:17]
	v_add_co_u32_e32 v12, vcc, s6, v12
	v_mul_f32_e32 v4, v4, v10
	s_nop 0
	v_addc_co_u32_e32 v13, vcc, 0, v13, vcc
	v_fmac_f32_e32 v48, v49, v4
	v_mov_b32_e32 v4, v174
	v_lshlrev_b32_e32 v11, 16, v11
	v_lshlrev_b32_e32 v8, 16, v8
	v_add_f32_e32 v8, v54, v8
	v_mul_f32_e32 v8, v8, v11
	v_bfe_u32 v11, v8, 16, 1
	v_add3_u32 v8, v8, v11, s5
	global_store_short_d16_hi v[12:13], v8, off offset:1536
	v_mul_f32_e32 v8, v9, v10
	v_fmac_f32_e32 v52, v53, v8
	v_mov_b32_e32 v8, v175
	v_mov_b32_e32 v9, v176
	v_lshlrev_b32_e32 v5, 16, v5
	v_add_f32_e32 v5, v50, v5
	v_lshlrev_b32_e32 v4, 16, v4
	v_add_f32_e32 v4, v48, v4
	v_lshlrev_b32_e32 v8, 16, v8
	v_add_f32_e32 v8, v52, v8
	v_lshlrev_b32_e32 v9, 16, v9
	v_mul_f32_e32 v8, v8, v9
	v_bfe_u32 v9, v8, 16, 1
	v_add3_u32 v8, v8, v9, s5
	global_store_short_d16_hi v[2:3], v8, off offset:32
	v_mov_b32_e32 v8, v177
	v_lshlrev_b32_e32 v8, 16, v8
	v_mul_f32_e32 v5, v5, v8
	v_bfe_u32 v8, v5, 16, 1
	v_add3_u32 v5, v5, v8, s5
	global_store_short_d16_hi v[2:3], v5, off offset:64
	v_mov_b32_e32 v5, v178
	v_lshlrev_b32_e32 v5, 16, v5
	v_mul_f32_e32 v4, v4, v5
	v_bfe_u32 v5, v4, 16, 1
	v_add3_u32 v4, v4, v5, s5
	global_store_short_d16_hi v[2:3], v4, off offset:96
	v_mov_b32_e32 v2, v0
	s_barrier
	s_nop 0
	v_cmp_eq_u32_e32 vcc, 0, v2
	s_and_saveexec_b64 s[0:1], vcc
	s_cbranch_execz .LBB0_1478
	v_readlane_b32 s6, v252, 14
	s_mov_b64 s[4:5], exec
	s_nop 0
	v_mov_b32_e32 v2, s6
	ds_write_b32 v2, v154
	v_mbcnt_lo_u32_b32 v2, s4, 0
	v_mbcnt_hi_u32_b32 v2, s5, v2
	v_cmp_eq_u32_e32 vcc, 0, v2
	s_and_saveexec_b64 s[6:7], vcc
	s_cbranch_execz .LBB0_1477
	s_bcnt1_i32_b64 s4, s[4:5]
	v_mov_b32_e32 v3, s4
	v_readlane_b32 s4, v253, 19
	v_readlane_b32 s5, v253, 20
	s_nop 4
	global_atomic_add v3, v83, v3, s[4:5] sc0
	s_branch .LBB0_1477
